# hand-written diff-attention epilogue + 5 nops after it so that every later loop head keeps its byte phase (attention loop head back on a 64-byte boundary)
# baseline (speedup 1.0000x reference)
.LBB0_563:
	v_mov_b32_e32 v230, 0xff800000
	v_mov_b32_e32 v228, v251
	v_mov_b32_e32 v229, v208
	s_nop 1
	v_permlane32_swap_b32_e32 v251, v228
	v_permlane32_swap_b32_e32 v208, v229
	v_add_f32_e32 v251, v251, v228
	v_add_f32_e32 v208, v208, v229
	s_or_b32 s14, s39, s35
	s_mul_hi_i32 s18, s14, 0x1a00
	s_mul_i32 s16, s14, 0x1a00
	v_div_scale_f32 v129, s[14:15], v251, v251, 1.0
	v_rcp_f32_e32 v130, v129
	s_add_u32 s14, s36, s16
	v_div_scale_f32 v147, s[16:17], v208, v208, v232
	v_fma_f32 v131, -v129, v130, 1.0
	v_fmac_f32_e32 v130, v131, v130
	v_div_scale_f32 v131, vcc, 1.0, v251, 1.0
	v_rcp_f32_e32 v148, v147
	v_mul_f32_e32 v132, v131, v130
	v_fma_f32 v133, -v129, v132, v131
	v_fmac_f32_e32 v132, v133, v130
	v_fma_f32 v129, -v129, v132, v131
	v_fma_f32 v149, -v147, v148, 1.0
	v_div_fmas_f32 v129, v129, v130, v132
	v_fmac_f32_e32 v148, v149, v148
	v_div_scale_f32 v149, vcc, v232, v208, v232
	v_mul_f32_e32 v150, v149, v148
	v_fma_f32 v151, -v147, v150, v149
	v_fmac_f32_e32 v150, v151, v148
	v_fma_f32 v147, -v147, v150, v149
	v_div_fixup_f32 v129, v129, v251, 1.0
	v_ashrrev_i32_e32 v128, 5, v235
	v_lshl_add_u32 v146, v235, 2, s40
	v_div_fmas_f32 v147, v147, v148, v150
	ds_write_b32 v146, v129
	v_lshl_add_u32 v129, v128, 4, s40
	v_div_fixup_f32 v147, v147, v208, v232
	ds_read_b128 v[130:133], v129
	ds_read_b128 v[134:137], v129 offset:32
	ds_read_b128 v[138:141], v129 offset:64
	ds_read_b128 v[142:145], v129 offset:96
	ds_write_b32 v146, v147
	ds_read_b128 v[146:149], v129
	ds_read_b128 v[150:153], v129 offset:32
	ds_read_b128 v[154:157], v129 offset:64
	ds_read_b128 v[158:161], v129 offset:96
	s_addc_u32 s15, s37, s18
	s_waitcnt lgkmcnt(0)
	v_and_b32_e32 v199, 31, v235
	v_lshlrev_b32_e32 v198, 2, v199
	global_load_dword v194, v198, s[4:5]
	global_load_dword v195, v198, s[4:5] offset:128
	global_load_dword v196, v198, s[4:5] offset:256
	global_load_dword v197, v198, s[4:5] offset:384
	v_mul_f32_e32 v112, v112, v146
	v_mul_f32_e32 v113, v113, v147
	v_mul_f32_e32 v114, v114, v148
	v_mul_f32_e32 v115, v115, v149
	v_mul_f32_e32 v116, v116, v150
	v_mul_f32_e32 v117, v117, v151
	v_mul_f32_e32 v118, v118, v152
	v_mul_f32_e32 v119, v119, v153
	v_mul_f32_e32 v120, v120, v154
	v_mul_f32_e32 v121, v121, v155
	v_mul_f32_e32 v122, v122, v156
	v_mul_f32_e32 v123, v123, v157
	v_mul_f32_e32 v124, v124, v158
	v_mul_f32_e32 v125, v125, v159
	v_mul_f32_e32 v126, v126, v160
	v_mul_f32_e32 v127, v127, v161
	v_fma_f32 v64, v64, v130, -v112
	v_fma_f32 v65, v65, v131, -v113
	v_fma_f32 v66, v66, v132, -v114
	v_fma_f32 v67, v67, v133, -v115
	v_fma_f32 v68, v68, v134, -v116
	v_fma_f32 v69, v69, v135, -v117
	v_fma_f32 v70, v70, v136, -v118
	v_fma_f32 v71, v71, v137, -v119
	v_fma_f32 v72, v72, v138, -v120
	v_fma_f32 v73, v73, v139, -v121
	v_fma_f32 v74, v74, v140, -v122
	v_fma_f32 v75, v75, v141, -v123
	v_fma_f32 v76, v76, v142, -v124
	v_fma_f32 v77, v77, v143, -v125
	v_fma_f32 v78, v78, v144, -v126
	v_fma_f32 v79, v79, v145, -v127
	v_mul_f32_e32 v96, v96, v146
	v_mul_f32_e32 v97, v97, v147
	v_mul_f32_e32 v98, v98, v148
	v_mul_f32_e32 v99, v99, v149
	v_mul_f32_e32 v100, v100, v150
	v_mul_f32_e32 v101, v101, v151
	v_mul_f32_e32 v102, v102, v152
	v_mul_f32_e32 v103, v103, v153
	v_mul_f32_e32 v104, v104, v154
	v_mul_f32_e32 v105, v105, v155
	v_mul_f32_e32 v106, v106, v156
	v_mul_f32_e32 v107, v107, v157
	v_mul_f32_e32 v108, v108, v158
	v_mul_f32_e32 v109, v109, v159
	v_mul_f32_e32 v110, v110, v160
	v_mul_f32_e32 v111, v111, v161
	v_fma_f32 v32, v32, v130, -v96
	v_fma_f32 v33, v33, v131, -v97
	v_fma_f32 v34, v34, v132, -v98
	v_fma_f32 v35, v35, v133, -v99
	v_fma_f32 v36, v36, v134, -v100
	v_fma_f32 v37, v37, v135, -v101
	v_fma_f32 v38, v38, v136, -v102
	v_fma_f32 v39, v39, v137, -v103
	v_fma_f32 v40, v40, v138, -v104
	v_fma_f32 v41, v41, v139, -v105
	v_fma_f32 v42, v42, v140, -v106
	v_fma_f32 v43, v43, v141, -v107
	v_fma_f32 v44, v44, v142, -v108
	v_fma_f32 v45, v45, v143, -v109
	v_fma_f32 v46, v46, v144, -v110
	v_fma_f32 v47, v47, v145, -v111
	v_mul_f32_e32 v80, v80, v146
	v_mul_f32_e32 v81, v81, v147
	v_mul_f32_e32 v82, v82, v148
	v_mul_f32_e32 v83, v83, v149
	v_mul_f32_e32 v84, v84, v150
	v_mul_f32_e32 v85, v85, v151
	v_mul_f32_e32 v86, v86, v152
	v_mul_f32_e32 v87, v87, v153
	v_mul_f32_e32 v88, v88, v154
	v_mul_f32_e32 v89, v89, v155
	v_mul_f32_e32 v90, v90, v156
	v_mul_f32_e32 v91, v91, v157
	v_mul_f32_e32 v92, v92, v158
	v_mul_f32_e32 v93, v93, v159
	v_mul_f32_e32 v94, v94, v160
	v_mul_f32_e32 v95, v95, v161
	v_fma_f32 v16, v16, v130, -v80
	v_fma_f32 v17, v17, v131, -v81
	v_fma_f32 v18, v18, v132, -v82
	v_fma_f32 v19, v19, v133, -v83
	v_fma_f32 v20, v20, v134, -v84
	v_fma_f32 v21, v21, v135, -v85
	v_fma_f32 v22, v22, v136, -v86
	v_fma_f32 v23, v23, v137, -v87
	v_fma_f32 v24, v24, v138, -v88
	v_fma_f32 v25, v25, v139, -v89
	v_fma_f32 v26, v26, v140, -v90
	v_fma_f32 v27, v27, v141, -v91
	v_fma_f32 v28, v28, v142, -v92
	v_fma_f32 v29, v29, v143, -v93
	v_fma_f32 v30, v30, v144, -v94
	v_fma_f32 v31, v31, v145, -v95
	v_mul_f32_e32 v48, v48, v146
	v_mul_f32_e32 v49, v49, v147
	v_mul_f32_e32 v50, v50, v148
	v_mul_f32_e32 v51, v51, v149
	v_mul_f32_e32 v52, v52, v150
	v_mul_f32_e32 v53, v53, v151
	v_mul_f32_e32 v54, v54, v152
	v_mul_f32_e32 v55, v55, v153
	v_mul_f32_e32 v56, v56, v154
	v_mul_f32_e32 v57, v57, v155
	v_mul_f32_e32 v58, v58, v156
	v_mul_f32_e32 v59, v59, v157
	v_mul_f32_e32 v60, v60, v158
	v_mul_f32_e32 v61, v61, v159
	v_mul_f32_e32 v62, v62, v160
	v_mul_f32_e32 v63, v63, v161
	v_fma_f32 v0, v0, v130, -v48
	v_fma_f32 v1, v1, v131, -v49
	v_fma_f32 v2, v2, v132, -v50
	v_fma_f32 v3, v3, v133, -v51
	v_fma_f32 v4, v4, v134, -v52
	v_fma_f32 v5, v5, v135, -v53
	v_fma_f32 v6, v6, v136, -v54
	v_fma_f32 v7, v7, v137, -v55
	v_fma_f32 v8, v8, v138, -v56
	v_fma_f32 v9, v9, v139, -v57
	v_fma_f32 v10, v10, v140, -v58
	v_fma_f32 v11, v11, v141, -v59
	v_fma_f32 v12, v12, v142, -v60
	v_fma_f32 v13, v13, v143, -v61
	v_fma_f32 v14, v14, v144, -v62
	v_fma_f32 v15, v15, v145, -v63
	v_mul_f32_e32 v162, v32, v32
	v_mul_f32_e32 v163, v33, v33
	v_mul_f32_e32 v164, v34, v34
	v_mul_f32_e32 v165, v35, v35
	v_mul_f32_e32 v166, v36, v36
	v_mul_f32_e32 v167, v37, v37
	v_mul_f32_e32 v168, v38, v38
	v_mul_f32_e32 v169, v39, v39
	v_mul_f32_e32 v170, v40, v40
	v_mul_f32_e32 v171, v41, v41
	v_mul_f32_e32 v172, v42, v42
	v_mul_f32_e32 v173, v43, v43
	v_mul_f32_e32 v174, v44, v44
	v_mul_f32_e32 v175, v45, v45
	v_mul_f32_e32 v176, v46, v46
	v_mul_f32_e32 v177, v47, v47
	v_fmac_f32_e32 v162, v64, v64
	v_fmac_f32_e32 v163, v65, v65
	v_fmac_f32_e32 v164, v66, v66
	v_fmac_f32_e32 v165, v67, v67
	v_fmac_f32_e32 v166, v68, v68
	v_fmac_f32_e32 v167, v69, v69
	v_fmac_f32_e32 v168, v70, v70
	v_fmac_f32_e32 v169, v71, v71
	v_fmac_f32_e32 v170, v72, v72
	v_fmac_f32_e32 v171, v73, v73
	v_fmac_f32_e32 v172, v74, v74
	v_fmac_f32_e32 v173, v75, v75
	v_fmac_f32_e32 v174, v76, v76
	v_fmac_f32_e32 v175, v77, v77
	v_fmac_f32_e32 v176, v78, v78
	v_fmac_f32_e32 v177, v79, v79
	v_fmac_f32_e32 v162, v16, v16
	v_fmac_f32_e32 v163, v17, v17
	v_fmac_f32_e32 v164, v18, v18
	v_fmac_f32_e32 v165, v19, v19
	v_fmac_f32_e32 v166, v20, v20
	v_fmac_f32_e32 v167, v21, v21
	v_fmac_f32_e32 v168, v22, v22
	v_fmac_f32_e32 v169, v23, v23
	v_fmac_f32_e32 v170, v24, v24
	v_fmac_f32_e32 v171, v25, v25
	v_fmac_f32_e32 v172, v26, v26
	v_fmac_f32_e32 v173, v27, v27
	v_fmac_f32_e32 v174, v28, v28
	v_fmac_f32_e32 v175, v29, v29
	v_fmac_f32_e32 v176, v30, v30
	v_fmac_f32_e32 v177, v31, v31
	v_fmac_f32_e32 v162, v0, v0
	v_fmac_f32_e32 v163, v1, v1
	v_fmac_f32_e32 v164, v2, v2
	v_fmac_f32_e32 v165, v3, v3
	v_fmac_f32_e32 v166, v4, v4
	v_fmac_f32_e32 v167, v5, v5
	v_fmac_f32_e32 v168, v6, v6
	v_fmac_f32_e32 v169, v7, v7
	v_fmac_f32_e32 v170, v8, v8
	v_fmac_f32_e32 v171, v9, v9
	v_fmac_f32_e32 v172, v10, v10
	v_fmac_f32_e32 v173, v11, v11
	v_fmac_f32_e32 v174, v12, v12
	v_fmac_f32_e32 v175, v13, v13
	v_fmac_f32_e32 v176, v14, v14
	v_fmac_f32_e32 v177, v15, v15
	v_add_f32_dpp v162, v162, v162 quad_perm:[1,0,3,2] row_mask:0xf bank_mask:0xf
	v_add_f32_dpp v163, v163, v163 quad_perm:[1,0,3,2] row_mask:0xf bank_mask:0xf
	v_add_f32_dpp v164, v164, v164 quad_perm:[1,0,3,2] row_mask:0xf bank_mask:0xf
	v_add_f32_dpp v165, v165, v165 quad_perm:[1,0,3,2] row_mask:0xf bank_mask:0xf
	v_add_f32_dpp v166, v166, v166 quad_perm:[1,0,3,2] row_mask:0xf bank_mask:0xf
	v_add_f32_dpp v167, v167, v167 quad_perm:[1,0,3,2] row_mask:0xf bank_mask:0xf
	v_add_f32_dpp v168, v168, v168 quad_perm:[1,0,3,2] row_mask:0xf bank_mask:0xf
	v_add_f32_dpp v169, v169, v169 quad_perm:[1,0,3,2] row_mask:0xf bank_mask:0xf
	v_add_f32_dpp v170, v170, v170 quad_perm:[1,0,3,2] row_mask:0xf bank_mask:0xf
	v_add_f32_dpp v171, v171, v171 quad_perm:[1,0,3,2] row_mask:0xf bank_mask:0xf
	v_add_f32_dpp v172, v172, v172 quad_perm:[1,0,3,2] row_mask:0xf bank_mask:0xf
	v_add_f32_dpp v173, v173, v173 quad_perm:[1,0,3,2] row_mask:0xf bank_mask:0xf
	v_add_f32_dpp v174, v174, v174 quad_perm:[1,0,3,2] row_mask:0xf bank_mask:0xf
	v_add_f32_dpp v175, v175, v175 quad_perm:[1,0,3,2] row_mask:0xf bank_mask:0xf
	v_add_f32_dpp v176, v176, v176 quad_perm:[1,0,3,2] row_mask:0xf bank_mask:0xf
	v_add_f32_dpp v177, v177, v177 quad_perm:[1,0,3,2] row_mask:0xf bank_mask:0xf
	v_add_f32_dpp v162, v162, v162 quad_perm:[2,3,0,1] row_mask:0xf bank_mask:0xf
	v_add_f32_dpp v163, v163, v163 quad_perm:[2,3,0,1] row_mask:0xf bank_mask:0xf
	v_add_f32_dpp v164, v164, v164 quad_perm:[2,3,0,1] row_mask:0xf bank_mask:0xf
	v_add_f32_dpp v165, v165, v165 quad_perm:[2,3,0,1] row_mask:0xf bank_mask:0xf
	v_add_f32_dpp v166, v166, v166 quad_perm:[2,3,0,1] row_mask:0xf bank_mask:0xf
	v_add_f32_dpp v167, v167, v167 quad_perm:[2,3,0,1] row_mask:0xf bank_mask:0xf
	v_add_f32_dpp v168, v168, v168 quad_perm:[2,3,0,1] row_mask:0xf bank_mask:0xf
	v_add_f32_dpp v169, v169, v169 quad_perm:[2,3,0,1] row_mask:0xf bank_mask:0xf
	v_add_f32_dpp v170, v170, v170 quad_perm:[2,3,0,1] row_mask:0xf bank_mask:0xf
	v_add_f32_dpp v171, v171, v171 quad_perm:[2,3,0,1] row_mask:0xf bank_mask:0xf
	v_add_f32_dpp v172, v172, v172 quad_perm:[2,3,0,1] row_mask:0xf bank_mask:0xf
	v_add_f32_dpp v173, v173, v173 quad_perm:[2,3,0,1] row_mask:0xf bank_mask:0xf
	v_add_f32_dpp v174, v174, v174 quad_perm:[2,3,0,1] row_mask:0xf bank_mask:0xf
	v_add_f32_dpp v175, v175, v175 quad_perm:[2,3,0,1] row_mask:0xf bank_mask:0xf
	v_add_f32_dpp v176, v176, v176 quad_perm:[2,3,0,1] row_mask:0xf bank_mask:0xf
	v_add_f32_dpp v177, v177, v177 quad_perm:[2,3,0,1] row_mask:0xf bank_mask:0xf
	v_add_f32_dpp v162, v162, v162 row_half_mirror row_mask:0xf bank_mask:0xf
	v_add_f32_dpp v163, v163, v163 row_half_mirror row_mask:0xf bank_mask:0xf
	v_add_f32_dpp v164, v164, v164 row_half_mirror row_mask:0xf bank_mask:0xf
	v_add_f32_dpp v165, v165, v165 row_half_mirror row_mask:0xf bank_mask:0xf
	v_add_f32_dpp v166, v166, v166 row_half_mirror row_mask:0xf bank_mask:0xf
	v_add_f32_dpp v167, v167, v167 row_half_mirror row_mask:0xf bank_mask:0xf
	v_add_f32_dpp v168, v168, v168 row_half_mirror row_mask:0xf bank_mask:0xf
	v_add_f32_dpp v169, v169, v169 row_half_mirror row_mask:0xf bank_mask:0xf
	v_add_f32_dpp v170, v170, v170 row_half_mirror row_mask:0xf bank_mask:0xf
	v_add_f32_dpp v171, v171, v171 row_half_mirror row_mask:0xf bank_mask:0xf
	v_add_f32_dpp v172, v172, v172 row_half_mirror row_mask:0xf bank_mask:0xf
	v_add_f32_dpp v173, v173, v173 row_half_mirror row_mask:0xf bank_mask:0xf
	v_add_f32_dpp v174, v174, v174 row_half_mirror row_mask:0xf bank_mask:0xf
	v_add_f32_dpp v175, v175, v175 row_half_mirror row_mask:0xf bank_mask:0xf
	v_add_f32_dpp v176, v176, v176 row_half_mirror row_mask:0xf bank_mask:0xf
	v_add_f32_dpp v177, v177, v177 row_half_mirror row_mask:0xf bank_mask:0xf
	v_add_f32_dpp v162, v162, v162 row_mirror row_mask:0xf bank_mask:0xf
	v_add_f32_dpp v163, v163, v163 row_mirror row_mask:0xf bank_mask:0xf
	v_add_f32_dpp v164, v164, v164 row_mirror row_mask:0xf bank_mask:0xf
	v_add_f32_dpp v165, v165, v165 row_mirror row_mask:0xf bank_mask:0xf
	v_add_f32_dpp v166, v166, v166 row_mirror row_mask:0xf bank_mask:0xf
	v_add_f32_dpp v167, v167, v167 row_mirror row_mask:0xf bank_mask:0xf
	v_add_f32_dpp v168, v168, v168 row_mirror row_mask:0xf bank_mask:0xf
	v_add_f32_dpp v169, v169, v169 row_mirror row_mask:0xf bank_mask:0xf
	v_add_f32_dpp v170, v170, v170 row_mirror row_mask:0xf bank_mask:0xf
	v_add_f32_dpp v171, v171, v171 row_mirror row_mask:0xf bank_mask:0xf
	v_add_f32_dpp v172, v172, v172 row_mirror row_mask:0xf bank_mask:0xf
	v_add_f32_dpp v173, v173, v173 row_mirror row_mask:0xf bank_mask:0xf
	v_add_f32_dpp v174, v174, v174 row_mirror row_mask:0xf bank_mask:0xf
	v_add_f32_dpp v175, v175, v175 row_mirror row_mask:0xf bank_mask:0xf
	v_add_f32_dpp v176, v176, v176 row_mirror row_mask:0xf bank_mask:0xf
	v_add_f32_dpp v177, v177, v177 row_mirror row_mask:0xf bank_mask:0xf
	v_mov_b32_e32 v178, v162
	v_mov_b32_e32 v179, v163
	v_mov_b32_e32 v180, v164
	v_mov_b32_e32 v181, v165
	v_mov_b32_e32 v182, v166
	v_mov_b32_e32 v183, v167
	v_mov_b32_e32 v184, v168
	v_mov_b32_e32 v185, v169
	v_mov_b32_e32 v186, v170
	v_mov_b32_e32 v187, v171
	v_mov_b32_e32 v188, v172
	v_mov_b32_e32 v189, v173
	v_mov_b32_e32 v190, v174
	v_mov_b32_e32 v191, v175
	v_mov_b32_e32 v192, v176
	v_mov_b32_e32 v193, v177
	v_permlane16_swap_b32_e32 v162, v178
	v_permlane16_swap_b32_e32 v163, v179
	v_permlane16_swap_b32_e32 v164, v180
	v_permlane16_swap_b32_e32 v165, v181
	v_permlane16_swap_b32_e32 v166, v182
	v_permlane16_swap_b32_e32 v167, v183
	v_permlane16_swap_b32_e32 v168, v184
	v_permlane16_swap_b32_e32 v169, v185
	v_permlane16_swap_b32_e32 v170, v186
	v_permlane16_swap_b32_e32 v171, v187
	v_permlane16_swap_b32_e32 v172, v188
	v_permlane16_swap_b32_e32 v173, v189
	v_permlane16_swap_b32_e32 v174, v190
	v_permlane16_swap_b32_e32 v175, v191
	v_permlane16_swap_b32_e32 v176, v192
	v_permlane16_swap_b32_e32 v177, v193
	v_add_f32_e32 v162, v162, v178
	v_add_f32_e32 v163, v163, v179
	v_add_f32_e32 v164, v164, v180
	v_add_f32_e32 v165, v165, v181
	v_add_f32_e32 v166, v166, v182
	v_add_f32_e32 v167, v167, v183
	v_add_f32_e32 v168, v168, v184
	v_add_f32_e32 v169, v169, v185
	v_add_f32_e32 v170, v170, v186
	v_add_f32_e32 v171, v171, v187
	v_add_f32_e32 v172, v172, v188
	v_add_f32_e32 v173, v173, v189
	v_add_f32_e32 v174, v174, v190
	v_add_f32_e32 v175, v175, v191
	v_add_f32_e32 v176, v176, v192
	v_add_f32_e32 v177, v177, v193
	v_fmamk_f32 v162, v162, 0x3c000000, v222
	v_fmamk_f32 v163, v163, 0x3c000000, v222
	v_fmamk_f32 v164, v164, 0x3c000000, v222
	v_fmamk_f32 v165, v165, 0x3c000000, v222
	v_fmamk_f32 v166, v166, 0x3c000000, v222
	v_fmamk_f32 v167, v167, 0x3c000000, v222
	v_fmamk_f32 v168, v168, 0x3c000000, v222
	v_fmamk_f32 v169, v169, 0x3c000000, v222
	v_fmamk_f32 v170, v170, 0x3c000000, v222
	v_fmamk_f32 v171, v171, 0x3c000000, v222
	v_fmamk_f32 v172, v172, 0x3c000000, v222
	v_fmamk_f32 v173, v173, 0x3c000000, v222
	v_fmamk_f32 v174, v174, 0x3c000000, v222
	v_fmamk_f32 v175, v175, 0x3c000000, v222
	v_fmamk_f32 v176, v176, 0x3c000000, v222
	v_fmamk_f32 v177, v177, 0x3c000000, v222
	v_rsq_f32_e32 v162, v162
	v_rsq_f32_e32 v163, v163
	v_rsq_f32_e32 v164, v164
	v_rsq_f32_e32 v165, v165
	v_rsq_f32_e32 v166, v166
	v_rsq_f32_e32 v167, v167
	v_rsq_f32_e32 v168, v168
	v_rsq_f32_e32 v169, v169
	v_rsq_f32_e32 v170, v170
	v_rsq_f32_e32 v171, v171
	v_rsq_f32_e32 v172, v172
	v_rsq_f32_e32 v173, v173
	v_rsq_f32_e32 v174, v174
	v_rsq_f32_e32 v175, v175
	v_rsq_f32_e32 v176, v176
	v_rsq_f32_e32 v177, v177
	s_waitcnt vmcnt(0)
	v_mul_f32_e32 v194, v233, v194
	v_mul_f32_e32 v195, v233, v195
	v_mul_f32_e32 v196, v233, v196
	v_mul_f32_e32 v197, v233, v197
	v_mul_f32_e32 v112, v194, v162
	v_mul_f32_e32 v113, v194, v163
	v_mul_f32_e32 v114, v194, v164
	v_mul_f32_e32 v115, v194, v165
	v_mul_f32_e32 v116, v194, v166
	v_mul_f32_e32 v117, v194, v167
	v_mul_f32_e32 v118, v194, v168
	v_mul_f32_e32 v119, v194, v169
	v_mul_f32_e32 v120, v194, v170
	v_mul_f32_e32 v121, v194, v171
	v_mul_f32_e32 v122, v194, v172
	v_mul_f32_e32 v123, v194, v173
	v_mul_f32_e32 v124, v194, v174
	v_mul_f32_e32 v125, v194, v175
	v_mul_f32_e32 v126, v194, v176
	v_mul_f32_e32 v127, v194, v177
	v_mul_f32_e32 v64, v64, v112
	v_mul_f32_e32 v65, v65, v113
	v_mul_f32_e32 v66, v66, v114
	v_mul_f32_e32 v67, v67, v115
	v_mul_f32_e32 v68, v68, v116
	v_mul_f32_e32 v69, v69, v117
	v_mul_f32_e32 v70, v70, v118
	v_mul_f32_e32 v71, v71, v119
	v_mul_f32_e32 v72, v72, v120
	v_mul_f32_e32 v73, v73, v121
	v_mul_f32_e32 v74, v74, v122
	v_mul_f32_e32 v75, v75, v123
	v_mul_f32_e32 v76, v76, v124
	v_mul_f32_e32 v77, v77, v125
	v_mul_f32_e32 v78, v78, v126
	v_mul_f32_e32 v79, v79, v127
	v_mul_f32_e32 v96, v195, v162
	v_mul_f32_e32 v97, v195, v163
	v_mul_f32_e32 v98, v195, v164
	v_mul_f32_e32 v99, v195, v165
	v_mul_f32_e32 v100, v195, v166
	v_mul_f32_e32 v101, v195, v167
	v_mul_f32_e32 v102, v195, v168
	v_mul_f32_e32 v103, v195, v169
	v_mul_f32_e32 v104, v195, v170
	v_mul_f32_e32 v105, v195, v171
	v_mul_f32_e32 v106, v195, v172
	v_mul_f32_e32 v107, v195, v173
	v_mul_f32_e32 v108, v195, v174
	v_mul_f32_e32 v109, v195, v175
	v_mul_f32_e32 v110, v195, v176
	v_mul_f32_e32 v111, v195, v177
	v_mul_f32_e32 v32, v32, v96
	v_mul_f32_e32 v33, v33, v97
	v_mul_f32_e32 v34, v34, v98
	v_mul_f32_e32 v35, v35, v99
	v_mul_f32_e32 v36, v36, v100
	v_mul_f32_e32 v37, v37, v101
	v_mul_f32_e32 v38, v38, v102
	v_mul_f32_e32 v39, v39, v103
	v_mul_f32_e32 v40, v40, v104
	v_mul_f32_e32 v41, v41, v105
	v_mul_f32_e32 v42, v42, v106
	v_mul_f32_e32 v43, v43, v107
	v_mul_f32_e32 v44, v44, v108
	v_mul_f32_e32 v45, v45, v109
	v_mul_f32_e32 v46, v46, v110
	v_mul_f32_e32 v47, v47, v111
	v_mul_f32_e32 v80, v196, v162
	v_mul_f32_e32 v81, v196, v163
	v_mul_f32_e32 v82, v196, v164
	v_mul_f32_e32 v83, v196, v165
	v_mul_f32_e32 v84, v196, v166
	v_mul_f32_e32 v85, v196, v167
	v_mul_f32_e32 v86, v196, v168
	v_mul_f32_e32 v87, v196, v169
	v_mul_f32_e32 v88, v196, v170
	v_mul_f32_e32 v89, v196, v171
	v_mul_f32_e32 v90, v196, v172
	v_mul_f32_e32 v91, v196, v173
	v_mul_f32_e32 v92, v196, v174
	v_mul_f32_e32 v93, v196, v175
	v_mul_f32_e32 v94, v196, v176
	v_mul_f32_e32 v95, v196, v177
	v_mul_f32_e32 v16, v16, v80
	v_mul_f32_e32 v17, v17, v81
	v_mul_f32_e32 v18, v18, v82
	v_mul_f32_e32 v19, v19, v83
	v_mul_f32_e32 v20, v20, v84
	v_mul_f32_e32 v21, v21, v85
	v_mul_f32_e32 v22, v22, v86
	v_mul_f32_e32 v23, v23, v87
	v_mul_f32_e32 v24, v24, v88
	v_mul_f32_e32 v25, v25, v89
	v_mul_f32_e32 v26, v26, v90
	v_mul_f32_e32 v27, v27, v91
	v_mul_f32_e32 v28, v28, v92
	v_mul_f32_e32 v29, v29, v93
	v_mul_f32_e32 v30, v30, v94
	v_mul_f32_e32 v31, v31, v95
	v_mul_f32_e32 v48, v197, v162
	v_mul_f32_e32 v49, v197, v163
	v_mul_f32_e32 v50, v197, v164
	v_mul_f32_e32 v51, v197, v165
	v_mul_f32_e32 v52, v197, v166
	v_mul_f32_e32 v53, v197, v167
	v_mul_f32_e32 v54, v197, v168
	v_mul_f32_e32 v55, v197, v169
	v_mul_f32_e32 v56, v197, v170
	v_mul_f32_e32 v57, v197, v171
	v_mul_f32_e32 v58, v197, v172
	v_mul_f32_e32 v59, v197, v173
	v_mul_f32_e32 v60, v197, v174
	v_mul_f32_e32 v61, v197, v175
	v_mul_f32_e32 v62, v197, v176
	v_mul_f32_e32 v63, v197, v177
	v_mul_f32_e32 v0, v0, v48
	v_mul_f32_e32 v1, v1, v49
	v_mul_f32_e32 v2, v2, v50
	v_mul_f32_e32 v3, v3, v51
	v_mul_f32_e32 v4, v4, v52
	v_mul_f32_e32 v5, v5, v53
	v_mul_f32_e32 v6, v6, v54
	v_mul_f32_e32 v7, v7, v55
	v_mul_f32_e32 v8, v8, v56
	v_mul_f32_e32 v9, v9, v57
	v_mul_f32_e32 v10, v10, v58
	v_mul_f32_e32 v11, v11, v59
	v_mul_f32_e32 v12, v12, v60
	v_mul_f32_e32 v13, v13, v61
	v_mul_f32_e32 v14, v14, v62
	v_mul_f32_e32 v15, v15, v63
	v_bfe_u32 v112, v64, 16, 1
	v_bfe_u32 v113, v65, 16, 1
	v_bfe_u32 v114, v66, 16, 1
	v_bfe_u32 v115, v67, 16, 1
	v_bfe_u32 v116, v68, 16, 1
	v_bfe_u32 v117, v69, 16, 1
	v_bfe_u32 v118, v70, 16, 1
	v_bfe_u32 v119, v71, 16, 1
	v_bfe_u32 v120, v72, 16, 1
	v_bfe_u32 v121, v73, 16, 1
	v_bfe_u32 v122, v74, 16, 1
	v_bfe_u32 v123, v75, 16, 1
	v_bfe_u32 v124, v76, 16, 1
	v_bfe_u32 v125, v77, 16, 1
	v_bfe_u32 v126, v78, 16, 1
	v_bfe_u32 v127, v79, 16, 1
	v_add3_u32 v64, v64, v112, s63
	v_add3_u32 v65, v65, v113, s63
	v_add3_u32 v66, v66, v114, s63
	v_add3_u32 v67, v67, v115, s63
	v_add3_u32 v68, v68, v116, s63
	v_add3_u32 v69, v69, v117, s63
	v_add3_u32 v70, v70, v118, s63
	v_add3_u32 v71, v71, v119, s63
	v_add3_u32 v72, v72, v120, s63
	v_add3_u32 v73, v73, v121, s63
	v_add3_u32 v74, v74, v122, s63
	v_add3_u32 v75, v75, v123, s63
	v_add3_u32 v76, v76, v124, s63
	v_add3_u32 v77, v77, v125, s63
	v_add3_u32 v78, v78, v126, s63
	v_add3_u32 v79, v79, v127, s63
	v_bfe_u32 v96, v32, 16, 1
	v_bfe_u32 v97, v33, 16, 1
	v_bfe_u32 v98, v34, 16, 1
	v_bfe_u32 v99, v35, 16, 1
	v_bfe_u32 v100, v36, 16, 1
	v_bfe_u32 v101, v37, 16, 1
	v_bfe_u32 v102, v38, 16, 1
	v_bfe_u32 v103, v39, 16, 1
	v_bfe_u32 v104, v40, 16, 1
	v_bfe_u32 v105, v41, 16, 1
	v_bfe_u32 v106, v42, 16, 1
	v_bfe_u32 v107, v43, 16, 1
	v_bfe_u32 v108, v44, 16, 1
	v_bfe_u32 v109, v45, 16, 1
	v_bfe_u32 v110, v46, 16, 1
	v_bfe_u32 v111, v47, 16, 1
	v_add3_u32 v32, v32, v96, s63
	v_add3_u32 v33, v33, v97, s63
	v_add3_u32 v34, v34, v98, s63
	v_add3_u32 v35, v35, v99, s63
	v_add3_u32 v36, v36, v100, s63
	v_add3_u32 v37, v37, v101, s63
	v_add3_u32 v38, v38, v102, s63
	v_add3_u32 v39, v39, v103, s63
	v_add3_u32 v40, v40, v104, s63
	v_add3_u32 v41, v41, v105, s63
	v_add3_u32 v42, v42, v106, s63
	v_add3_u32 v43, v43, v107, s63
	v_add3_u32 v44, v44, v108, s63
	v_add3_u32 v45, v45, v109, s63
	v_add3_u32 v46, v46, v110, s63
	v_add3_u32 v47, v47, v111, s63
	v_bfe_u32 v80, v16, 16, 1
	v_bfe_u32 v81, v17, 16, 1
	v_bfe_u32 v82, v18, 16, 1
	v_bfe_u32 v83, v19, 16, 1
	v_bfe_u32 v84, v20, 16, 1
	v_bfe_u32 v85, v21, 16, 1
	v_bfe_u32 v86, v22, 16, 1
	v_bfe_u32 v87, v23, 16, 1
	v_bfe_u32 v88, v24, 16, 1
	v_bfe_u32 v89, v25, 16, 1
	v_bfe_u32 v90, v26, 16, 1
	v_bfe_u32 v91, v27, 16, 1
	v_bfe_u32 v92, v28, 16, 1
	v_bfe_u32 v93, v29, 16, 1
	v_bfe_u32 v94, v30, 16, 1
	v_bfe_u32 v95, v31, 16, 1
	v_add3_u32 v16, v16, v80, s63
	v_add3_u32 v17, v17, v81, s63
	v_add3_u32 v18, v18, v82, s63
	v_add3_u32 v19, v19, v83, s63
	v_add3_u32 v20, v20, v84, s63
	v_add3_u32 v21, v21, v85, s63
	v_add3_u32 v22, v22, v86, s63
	v_add3_u32 v23, v23, v87, s63
	v_add3_u32 v24, v24, v88, s63
	v_add3_u32 v25, v25, v89, s63
	v_add3_u32 v26, v26, v90, s63
	v_add3_u32 v27, v27, v91, s63
	v_add3_u32 v28, v28, v92, s63
	v_add3_u32 v29, v29, v93, s63
	v_add3_u32 v30, v30, v94, s63
	v_add3_u32 v31, v31, v95, s63
	v_bfe_u32 v48, v0, 16, 1
	v_bfe_u32 v49, v1, 16, 1
	v_bfe_u32 v50, v2, 16, 1
	v_bfe_u32 v51, v3, 16, 1
	v_bfe_u32 v52, v4, 16, 1
	v_bfe_u32 v53, v5, 16, 1
	v_bfe_u32 v54, v6, 16, 1
	v_bfe_u32 v55, v7, 16, 1
	v_bfe_u32 v56, v8, 16, 1
	v_bfe_u32 v57, v9, 16, 1
	v_bfe_u32 v58, v10, 16, 1
	v_bfe_u32 v59, v11, 16, 1
	v_bfe_u32 v60, v12, 16, 1
	v_bfe_u32 v61, v13, 16, 1
	v_bfe_u32 v62, v14, 16, 1
	v_bfe_u32 v63, v15, 16, 1
	v_add3_u32 v0, v0, v48, s63
	v_add3_u32 v1, v1, v49, s63
	v_add3_u32 v2, v2, v50, s63
	v_add3_u32 v3, v3, v51, s63
	v_add3_u32 v4, v4, v52, s63
	v_add3_u32 v5, v5, v53, s63
	v_add3_u32 v6, v6, v54, s63
	v_add3_u32 v7, v7, v55, s63
	v_add3_u32 v8, v8, v56, s63
	v_add3_u32 v9, v9, v57, s63
	v_add3_u32 v10, v10, v58, s63
	v_add3_u32 v11, v11, v59, s63
	v_add3_u32 v12, v12, v60, s63
	v_add3_u32 v13, v13, v61, s63
	v_add3_u32 v14, v14, v62, s63
	v_add3_u32 v15, v15, v63, s63
	s_lshl_b32 s16, s38, 8
	s_add_i32 s16, s16, s65
	v_lshlrev_b32_e32 v200, 10, v128
	v_lshl_add_u32 v200, v199, 1, v200
	v_add_u32_e32 v200, s16, v200
	ds_write_b16_d16_hi v200, v64 offset:0
	ds_write_b16_d16_hi v200, v32 offset:64
	ds_write_b16_d16_hi v200, v16 offset:128
	ds_write_b16_d16_hi v200, v0 offset:192
	ds_write_b16_d16_hi v200, v65 offset:256
	ds_write_b16_d16_hi v200, v33 offset:320
	ds_write_b16_d16_hi v200, v17 offset:384
	ds_write_b16_d16_hi v200, v1 offset:448
	ds_write_b16_d16_hi v200, v66 offset:512
	ds_write_b16_d16_hi v200, v34 offset:576
	ds_write_b16_d16_hi v200, v18 offset:640
	ds_write_b16_d16_hi v200, v2 offset:704
	ds_write_b16_d16_hi v200, v67 offset:768
	ds_write_b16_d16_hi v200, v35 offset:832
	ds_write_b16_d16_hi v200, v19 offset:896
	ds_write_b16_d16_hi v200, v3 offset:960
	ds_write_b16_d16_hi v200, v68 offset:2048
	ds_write_b16_d16_hi v200, v36 offset:2112
	ds_write_b16_d16_hi v200, v20 offset:2176
	ds_write_b16_d16_hi v200, v4 offset:2240
	ds_write_b16_d16_hi v200, v69 offset:2304
	ds_write_b16_d16_hi v200, v37 offset:2368
	ds_write_b16_d16_hi v200, v21 offset:2432
	ds_write_b16_d16_hi v200, v5 offset:2496
	ds_write_b16_d16_hi v200, v70 offset:2560
	ds_write_b16_d16_hi v200, v38 offset:2624
	ds_write_b16_d16_hi v200, v22 offset:2688
	ds_write_b16_d16_hi v200, v6 offset:2752
	ds_write_b16_d16_hi v200, v71 offset:2816
	ds_write_b16_d16_hi v200, v39 offset:2880
	ds_write_b16_d16_hi v200, v23 offset:2944
	ds_write_b16_d16_hi v200, v7 offset:3008
	ds_write_b16_d16_hi v200, v72 offset:4096
	ds_write_b16_d16_hi v200, v40 offset:4160
	ds_write_b16_d16_hi v200, v24 offset:4224
	ds_write_b16_d16_hi v200, v8 offset:4288
	ds_write_b16_d16_hi v200, v73 offset:4352
	ds_write_b16_d16_hi v200, v41 offset:4416
	ds_write_b16_d16_hi v200, v25 offset:4480
	ds_write_b16_d16_hi v200, v9 offset:4544
	ds_write_b16_d16_hi v200, v74 offset:4608
	ds_write_b16_d16_hi v200, v42 offset:4672
	ds_write_b16_d16_hi v200, v26 offset:4736
	ds_write_b16_d16_hi v200, v10 offset:4800
	ds_write_b16_d16_hi v200, v75 offset:4864
	ds_write_b16_d16_hi v200, v43 offset:4928
	ds_write_b16_d16_hi v200, v27 offset:4992
	ds_write_b16_d16_hi v200, v11 offset:5056
	ds_write_b16_d16_hi v200, v76 offset:6144
	ds_write_b16_d16_hi v200, v44 offset:6208
	ds_write_b16_d16_hi v200, v28 offset:6272
	ds_write_b16_d16_hi v200, v12 offset:6336
	ds_write_b16_d16_hi v200, v77 offset:6400
	ds_write_b16_d16_hi v200, v45 offset:6464
	ds_write_b16_d16_hi v200, v29 offset:6528
	ds_write_b16_d16_hi v200, v13 offset:6592
	ds_write_b16_d16_hi v200, v78 offset:6656
	ds_write_b16_d16_hi v200, v46 offset:6720
	ds_write_b16_d16_hi v200, v30 offset:6784
	ds_write_b16_d16_hi v200, v14 offset:6848
	ds_write_b16_d16_hi v200, v79 offset:6912
	ds_write_b16_d16_hi v200, v47 offset:6976
	ds_write_b16_d16_hi v200, v31 offset:7040
	ds_write_b16_d16_hi v200, v15 offset:7104
	v_lshrrev_b32_e32 v201, 4, v235
	v_and_b32_e32 v204, 15, v235
	v_lshlrev_b32_e32 v208, 4, v204
	v_lshl_add_u32 v205, v201, 8, v208
	v_add_u32_e32 v205, s16, v205
	v_add_u32_e32 v206, s38, v201
	v_lshl_add_u64 v[202:203], s[14:15], 0, v[208:209]
	v_mad_i64_i32 v[202:203], s[16:17], v206, s62, v[202:203]
	s_lshl_b32 s16, s62, 2
	s_mov_b32 s17, 0
	ds_read_b128 v[96:99], v205 offset:0
	ds_read_b128 v[100:103], v205 offset:1024
	ds_read_b128 v[104:107], v205 offset:2048
	ds_read_b128 v[108:111], v205 offset:3072
	ds_read_b128 v[112:115], v205 offset:4096
	ds_read_b128 v[116:119], v205 offset:5120
	ds_read_b128 v[120:123], v205 offset:6144
	ds_read_b128 v[124:127], v205 offset:7168
	s_waitcnt lgkmcnt(7)
	global_store_dwordx4 v[202:203], v[96:99], off
	v_lshl_add_u64 v[202:203], v[202:203], 0, s[16:17]
	s_waitcnt lgkmcnt(6)
	global_store_dwordx4 v[202:203], v[100:103], off
	v_lshl_add_u64 v[202:203], v[202:203], 0, s[16:17]
	s_waitcnt lgkmcnt(5)
	global_store_dwordx4 v[202:203], v[104:107], off
	v_lshl_add_u64 v[202:203], v[202:203], 0, s[16:17]
	s_waitcnt lgkmcnt(4)
	global_store_dwordx4 v[202:203], v[108:111], off
	v_lshl_add_u64 v[202:203], v[202:203], 0, s[16:17]
	s_waitcnt lgkmcnt(3)
	global_store_dwordx4 v[202:203], v[112:115], off
	v_lshl_add_u64 v[202:203], v[202:203], 0, s[16:17]
	s_waitcnt lgkmcnt(2)
	global_store_dwordx4 v[202:203], v[116:119], off
	v_lshl_add_u64 v[202:203], v[202:203], 0, s[16:17]
	s_waitcnt lgkmcnt(1)
	global_store_dwordx4 v[202:203], v[120:123], off
	v_lshl_add_u64 v[202:203], v[202:203], 0, s[16:17]
	s_waitcnt lgkmcnt(0)
	global_store_dwordx4 v[202:203], v[124:127], off
	s_mov_b64 s[14:15], 0
	s_and_b64 vcc, exec, s[12:13]
	s_waitcnt vmcnt(63) expcnt(7) lgkmcnt(15)
	s_barrier
	s_cbranch_vccnz .LBB0_559
	s_nop 0
	s_nop 0
	s_nop 0
	s_nop 0
	s_nop 0
